# chained top-half expert K-loops: removed hipcc's in-loop vmcnt register guards (they drained the DMA pipeline every iteration; everything older is retired by the preamble's vmcnt(0))
# speedup vs baseline: 1.0095x; 1.0095x over previous
; #define G_WAIT_V(n) asm volatile("s_waitcnt vmcnt(" #n ")" ::: "memory")
; #define G_BAR() __builtin_amdgcn_s_barrier()
; #define G_SCHED() __builtin_amdgcn_sched_barrier(0)
; #define D_STAGE_A(slot, half, kt) D_STAGE(rsA, voffA, slot, half, kt)
; #define D_STAGE_B(slot, half, kt) D_STAGE(rsB, voffB, slot, half, kt)
; #define D_LDA(dst, slot) do { _Pragma("unroll") for (int m = 0; m < 4; ++m) _Pragma("unroll") for (int k = 0; k < 2; ++k) \
;     dst[m][k] = *(const LDS_AS bf16x8*)(lds + (slot) + aoff + m * 2048 + k * 1024); } while (0)
; #define D_LDB(dst, slot) do { _Pragma("unroll") for (int n = 0; n < 2; ++n) _Pragma("unroll") for (int k = 0; k < 2; ++k) \
;     dst[n][k] = *(const LDS_AS bf16x8*)(lds + (slot) + boff + n * 2048 + k * 1024); } while (0)
; #define D_MMA(ai, bj, At, Bf) do { __builtin_amdgcn_s_setprio(1); _Pragma("unroll") for (int m = 0; m < 4; ++m) _Pragma("unroll") for (int n = 0; n < 2; ++n) _Pragma("unroll") for (int k = 0; k < 2; ++k) \
;     acc[ai][bj][m][n] = __builtin_amdgcn_mfma_f32_16x16x32_bf16(Bf[n][k], At[m][k], acc[ai][bj][m][n], 0, 0, 0); __builtin_amdgcn_s_setprio(0); } while (0)
; #define D_WAIT_L(n) asm volatile("s_waitcnt lgkmcnt(" #n ")" ::: "memory")
; #define D_STAGE_A(slot, half, kt) D_STAGE(rsA, voffA, slot, half, kt)
; #define D_STAGE_B(slot, half, kt) do { _Pragma("unroll") for (int _i = 0; _i < 2; ++_i) { const unsigned _m0 = ldsw + (unsigned)((slot) + _i * 8192); const unsigned _so = (unsigned)(kt) * 128u + (half) * bt_half + _i * bt_piece; \
;     asm volatile("s_mov_b32 m0, %0\n\ts_nop 4\n\tbuffer_load_dwordx4 %1, %2, %3 offen lds" :: "s"(_m0), "v"(voffB0), "s"(rsB), "s"(_so) : "m0", "memory"); } } while (0)
;     ...
;     D_LDB(B0, G_SB(0, 0)); G_SCHED(); D_LDA(At, G_SA(0, 0)); D_STAGE_A(G_SA(1, 1), 1, t1);
;     D_WAIT_L(8); G_BAR(); D_WAIT_L(0); G_SCHED(); D_MMA(0, 0, At, B0); G_BAR(); G_SCHED();
;     D_LDB(B1, G_SB(0, 1)); D_STAGE_B(G_SB(0, 0), 0, t2);
;     G_BAR(); D_WAIT_L(0); G_SCHED(); D_MMA(0, 1, At, B1); G_BAR(); G_SCHED();
;     D_LDA(At, G_SA(0, 1)); D_STAGE_A(G_SA(0, 0), 0, t2);
;     G_BAR(); D_WAIT_L(0); G_SCHED(); D_MMA(1, 0, At, B0); G_BAR(); G_SCHED();
;     D_STAGE_B(G_SB(0, 1), 1, t2);
;     G_WAIT_V(6); G_BAR(); G_SCHED(); D_MMA(1, 1, At, B1); G_BAR(); G_SCHED();
;     D_LDB(B0, G_SB(1, 0)); G_SCHED(); D_LDA(At, G_SA(1, 0)); D_STAGE_A(G_SA(0, 1), 1, t2);
.LBB0_1510:
	s_add_i32 s77, 0, 0x10010
	s_nop 0
	v_add_u32_e32 v73, s77, v68
	s_nop 0
	v_add_u32_e32 v86, s77, v69
	ds_read_b128 v[74:77], v73
	ds_read_b128 v[82:85], v73 offset:2048
	ds_read_b128 v[78:81], v86
	s_nop 0
	ds_read_b128 v[86:89], v86 offset:2048
	s_add_i32 s38, s75, 1
	s_add_i32 s74, s75, 3
	s_add_i32 s73, s75, 2
	s_add_i32 s82, 0, 0x14010
	s_cmp_lt_u32 s75, 14
	s_cselect_b32 s76, s73, s75
	s_cselect_b32 s38, s74, s38
	s_lshl_b32 s81, s76, 7
	s_lshl_b32 s76, s38, 7
	s_add_i32 s83, s81, 0x20000
	s_add_i32 s84, s81, 0x2000
	s_add_i32 s85, s81, 0x22000
	s_add_i32 s86, 0, 0x18010
	s_add_i32 s80, 0, 0x1c010
	s_add_i32 s79, s76, 0x20000
	s_add_i32 s77, s76, 0x2000
	s_add_i32 s78, s76, 0x22000
	s_add_i32 s74, s72, 0x100
	s_cmp_gt_u32 s75, 13
	s_nop 0
	ds_read_b128 v[90:93], v71 offset:16
	s_nop 0
	ds_read_b128 v[98:101], v71 offset:2064
	ds_read_b128 v[94:97], v72 offset:16
	s_nop 0
	ds_read_b128 v[102:105], v72 offset:2064
	s_nop 0
	ds_read_b128 v[106:109], v71 offset:4112
	s_nop 0
	ds_read_b128 v[114:117], v71 offset:6160
	ds_read_b128 v[110:113], v72 offset:4112
	s_nop 0
	ds_read_b128 v[118:121], v72 offset:6160
	s_waitcnt lgkmcnt(12)
	s_mov_b32 m0, s26
	s_nop 0
	buffer_load_dwordx4 v66, s[8:11], s72 offen lds
	s_nop 0
	s_mov_b32 m0, s62
	s_nop 0
	buffer_load_dwordx4 v67, s[8:11], s72 offen lds
	s_waitcnt lgkmcnt(8)
	s_waitcnt vmcnt(10)
	s_barrier
	s_nop 0
	s_setprio 1
	s_waitcnt lgkmcnt(5)
	v_mfma_scale_f32_16x16x128_f8f6f4 v[56:59], v[74:81], v[90:97], v[56:59], v149, v148 op_sel_hi:[0,0,0]
	v_mfma_scale_f32_16x16x128_f8f6f4 v[60:63], v[82:89], v[90:97], v[60:63], v149, v148 op_sel_hi:[0,0,0]
	s_waitcnt lgkmcnt(4)
	v_mfma_scale_f32_16x16x128_f8f6f4 v[44:47], v[74:81], v[98:105], v[44:47], v149, v148 op_sel_hi:[0,0,0]
	v_mfma_scale_f32_16x16x128_f8f6f4 v[40:43], v[82:89], v[98:105], v[40:43], v149, v148 op_sel_hi:[0,0,0]
	s_waitcnt lgkmcnt(1)
	v_mfma_scale_f32_16x16x128_f8f6f4 v[122:125], v[74:81], v[106:113], v[28:31], v149, v148 op_sel_hi:[0,0,0]
	v_mfma_scale_f32_16x16x128_f8f6f4 v[126:129], v[82:89], v[106:113], v[24:27], v149, v148 op_sel_hi:[0,0,0]
	s_waitcnt lgkmcnt(0)
	v_mfma_scale_f32_16x16x128_f8f6f4 v[130:133], v[74:81], v[114:121], v[12:15], v149, v148 op_sel_hi:[0,0,0]
	v_mfma_scale_f32_16x16x128_f8f6f4 v[134:137], v[82:89], v[114:121], v[8:11], v149, v148 op_sel_hi:[0,0,0]
	s_setprio 0
	s_barrier
	s_nop 3
	v_add_u32_e32 v12, s82, v68
	v_add_u32_e32 v28, s82, v69
	ds_read_b128 v[8:11], v12
	ds_read_b128 v[24:27], v12 offset:2048
	ds_read_b128 v[12:15], v28
	ds_read_b128 v[28:31], v28 offset:2048
	s_mov_b32 m0, s27
	s_nop 0
	buffer_load_dwordx4 v70, s[4:7], s81 offen lds
	s_nop 0
	s_mov_b32 m0, s63
	s_nop 0
	buffer_load_dwordx4 v70, s[4:7], s83 offen lds
	s_waitcnt vmcnt(10)
	s_barrier
	s_nop 0
	s_setprio 1
	s_waitcnt lgkmcnt(1)
	v_mfma_scale_f32_16x16x128_f8f6f4 v[52:55], v[8:15], v[90:97], v[52:55], v149, v148 op_sel_hi:[0,0,0]
	s_waitcnt lgkmcnt(0)
	v_mfma_scale_f32_16x16x128_f8f6f4 v[48:51], v[24:31], v[90:97], v[48:51], v149, v148 op_sel_hi:[0,0,0]
	v_mfma_scale_f32_16x16x128_f8f6f4 v[138:141], v[8:15], v[98:105], v[36:39], v149, v148 op_sel_hi:[0,0,0]
	v_mfma_scale_f32_16x16x128_f8f6f4 v[152:155], v[24:31], v[98:105], v[32:35], v149, v148 op_sel_hi:[0,0,0]
	v_mfma_scale_f32_16x16x128_f8f6f4 v[156:159], v[8:15], v[106:113], v[20:23], v149, v148 op_sel_hi:[0,0,0]
	v_mfma_scale_f32_16x16x128_f8f6f4 v[106:109], v[24:31], v[106:113], v[16:19], v149, v148 op_sel_hi:[0,0,0]
	v_mfma_scale_f32_16x16x128_f8f6f4 v[110:113], v[8:15], v[114:121], v[4:7], v149, v148 op_sel_hi:[0,0,0]
	v_mfma_scale_f32_16x16x128_f8f6f4 v[114:117], v[24:31], v[114:121], v[0:3], v149, v148 op_sel_hi:[0,0,0]
	s_setprio 0
	s_barrier
	s_mov_b32 m0, s17
	s_nop 0
	buffer_load_dwordx4 v64, s[8:11], s81 offen lds
	s_nop 0
	s_mov_b32 m0, s66
	s_nop 0
	buffer_load_dwordx4 v65, s[8:11], s81 offen lds
	s_barrier
; #define G_WAIT_V(n) asm volatile("s_waitcnt vmcnt(" #n ")" ::: "memory")
; #define G_BAR() __builtin_amdgcn_s_barrier()
; #define G_SCHED() __builtin_amdgcn_sched_barrier(0)
; #define D_STAGE_A(slot, half, kt) D_STAGE(rsA, voffA, slot, half, kt)
; #define D_STAGE_B(slot, half, kt) D_STAGE(rsB, voffB, slot, half, kt)
; #define D_LDA(dst, slot) do { _Pragma("unroll") for (int m = 0; m < 4; ++m) _Pragma("unroll") for (int k = 0; k < 2; ++k) \
;     dst[m][k] = *(const LDS_AS bf16x8*)(lds + (slot) + aoff + m * 2048 + k * 1024); } while (0)
; #define D_LDB(dst, slot) do { _Pragma("unroll") for (int n = 0; n < 2; ++n) _Pragma("unroll") for (int k = 0; k < 2; ++k) \
;     dst[n][k] = *(const LDS_AS bf16x8*)(lds + (slot) + boff + n * 2048 + k * 1024); } while (0)
; #define D_MMA(ai, bj, At, Bf) do { __builtin_amdgcn_s_setprio(1); _Pragma("unroll") for (int m = 0; m < 4; ++m) _Pragma("unroll") for (int n = 0; n < 2; ++n) _Pragma("unroll") for (int k = 0; k < 2; ++k) \
;     acc[ai][bj][m][n] = __builtin_amdgcn_mfma_f32_16x16x32_bf16(Bf[n][k], At[m][k], acc[ai][bj][m][n], 0, 0, 0); __builtin_amdgcn_s_setprio(0); } while (0)
; #define D_WAIT_L(n) asm volatile("s_waitcnt lgkmcnt(" #n ")" ::: "memory")
; #define D_STAGE_A(slot, half, kt) D_STAGE(rsA, voffA, slot, half, kt)
; #define D_STAGE_B(slot, half, kt) do { _Pragma("unroll") for (int _i = 0; _i < 2; ++_i) { const unsigned _m0 = ldsw + (unsigned)((slot) + _i * 8192); const unsigned _so = (unsigned)(kt) * 128u + (half) * bt_half + _i * bt_piece; \
;     asm volatile("s_mov_b32 m0, %0\n\ts_nop 4\n\tbuffer_load_dwordx4 %1, %2, %3 offen lds" :: "s"(_m0), "v"(voffB0), "s"(rsB), "s"(_so) : "m0", "memory"); } } while (0)
; #define D_WAIT_L(n) asm volatile("s_waitcnt lgkmcnt(" #n ")" ::: "memory")
;     ...
;     D_LDB(B0, G_SB(1, 0)); G_SCHED(); D_LDA(At, G_SA(1, 0)); D_STAGE_A(G_SA(0, 1), 1, t2);
;     D_WAIT_L(8); G_BAR(); D_WAIT_L(0); G_SCHED(); D_MMA(0, 0, At, B0); G_BAR(); G_SCHED();
;     D_LDB(B1, G_SB(1, 1)); D_STAGE_B(G_SB(1, 0), 0, t3);
;     G_BAR(); D_WAIT_L(0); G_SCHED(); D_MMA(0, 1, At, B1); G_BAR(); G_SCHED();
;     D_LDA(At, G_SA(1, 1)); D_STAGE_A(G_SA(1, 0), 0, t3);
;     G_BAR(); D_WAIT_L(0); G_SCHED(); D_MMA(1, 0, At, B0); G_BAR(); G_SCHED();
;     D_STAGE_B(G_SB(1, 1), 1, t3);
;     G_WAIT_V(6); G_BAR(); G_SCHED(); D_MMA(1, 1, At, B1); G_BAR(); G_SCHED();
;   }
	s_waitcnt lgkmcnt(0)
	s_barrier
	s_mov_b32 m0, s28
	s_nop 0
	buffer_load_dwordx4 v70, s[4:7], s84 offen lds
	s_nop 0
	s_mov_b32 m0, s67
	s_nop 0
	buffer_load_dwordx4 v70, s[4:7], s85 offen lds
	s_waitcnt vmcnt(10)
	s_barrier
	s_barrier
	v_add_u32_e32 v4, s86, v68
	v_add_u32_e32 v8, s86, v69
	ds_read_b128 v[0:3], v4
	ds_read_b128 v[16:19], v4 offset:2048
	ds_read_b128 v[4:7], v8
	ds_read_b128 v[20:23], v8 offset:2048
	ds_read_b128 v[32:35], v71 offset:32784
	ds_read_b128 v[74:77], v71 offset:34832
	ds_read_b128 v[36:39], v72 offset:32784
	ds_read_b128 v[78:81], v72 offset:34832
	ds_read_b128 v[82:85], v71 offset:36880
	ds_read_b128 v[90:93], v71 offset:38928
	ds_read_b128 v[86:89], v72 offset:36880
	ds_read_b128 v[94:97], v72 offset:38928
	s_mov_b32 m0, s29
	s_nop 0
	buffer_load_dwordx4 v66, s[8:11], s81 offen lds
	s_nop 0
	s_mov_b32 m0, s68
	s_nop 0
	buffer_load_dwordx4 v67, s[8:11], s81 offen lds
	s_waitcnt lgkmcnt(8)
	s_waitcnt vmcnt(10)
	s_barrier
	s_nop 0
	s_setprio 1
	s_waitcnt lgkmcnt(5)
	v_mfma_scale_f32_16x16x128_f8f6f4 v[56:59], v[0:7], v[32:39], v[56:59], v149, v148 op_sel_hi:[0,0,0]
	v_mfma_scale_f32_16x16x128_f8f6f4 v[60:63], v[16:23], v[32:39], v[60:63], v149, v148 op_sel_hi:[0,0,0]
	s_waitcnt lgkmcnt(4)
	v_mfma_scale_f32_16x16x128_f8f6f4 v[44:47], v[0:7], v[74:81], v[44:47], v149, v148 op_sel_hi:[0,0,0]
	v_mfma_scale_f32_16x16x128_f8f6f4 v[40:43], v[16:23], v[74:81], v[40:43], v149, v148 op_sel_hi:[0,0,0]
	s_waitcnt lgkmcnt(1)
	v_mfma_scale_f32_16x16x128_f8f6f4 v[28:31], v[0:7], v[82:89], v[122:125], v149, v148 op_sel_hi:[0,0,0]
	v_mfma_scale_f32_16x16x128_f8f6f4 v[24:27], v[16:23], v[82:89], v[126:129], v149, v148 op_sel_hi:[0,0,0]
	s_waitcnt lgkmcnt(0)
	v_mfma_scale_f32_16x16x128_f8f6f4 v[12:15], v[0:7], v[90:97], v[130:133], v149, v148 op_sel_hi:[0,0,0]
	v_mfma_scale_f32_16x16x128_f8f6f4 v[8:11], v[16:23], v[90:97], v[134:137], v149, v148 op_sel_hi:[0,0,0]
	s_setprio 0
	s_barrier
	v_add_u32_e32 v4, s80, v68
	v_add_u32_e32 v16, s80, v69
	ds_read_b128 v[0:3], v4
	ds_read_b128 v[98:101], v4 offset:2048
	ds_read_b128 v[4:7], v16
	ds_read_b128 v[102:105], v16 offset:2048
	s_mov_b32 m0, s39
	s_nop 0
	buffer_load_dwordx4 v70, s[4:7], s76 offen lds
	s_nop 0
	s_mov_b32 m0, s69
	s_nop 0
	buffer_load_dwordx4 v70, s[4:7], s79 offen lds
	s_waitcnt vmcnt(10)
	s_barrier
	s_nop 0
	s_setprio 1
	s_waitcnt lgkmcnt(1)
	v_mfma_scale_f32_16x16x128_f8f6f4 v[52:55], v[0:7], v[32:39], v[52:55], v149, v148 op_sel_hi:[0,0,0]
	s_waitcnt lgkmcnt(0)
	v_mfma_scale_f32_16x16x128_f8f6f4 v[48:51], v[98:105], v[32:39], v[48:51], v149, v148 op_sel_hi:[0,0,0]
	v_mfma_scale_f32_16x16x128_f8f6f4 v[36:39], v[0:7], v[74:81], v[138:141], v149, v148 op_sel_hi:[0,0,0]
	v_mfma_scale_f32_16x16x128_f8f6f4 v[32:35], v[98:105], v[74:81], v[152:155], v149, v148 op_sel_hi:[0,0,0]
	v_mfma_scale_f32_16x16x128_f8f6f4 v[20:23], v[0:7], v[82:89], v[156:159], v149, v148 op_sel_hi:[0,0,0]
	v_mfma_scale_f32_16x16x128_f8f6f4 v[16:19], v[98:105], v[82:89], v[106:109], v149, v148 op_sel_hi:[0,0,0]
	v_mfma_scale_f32_16x16x128_f8f6f4 v[4:7], v[0:7], v[90:97], v[110:113], v149, v148 op_sel_hi:[0,0,0]
	v_mfma_scale_f32_16x16x128_f8f6f4 v[0:3], v[98:105], v[90:97], v[114:117], v149, v148 op_sel_hi:[0,0,0]
	s_setprio 0
	s_barrier
	s_mov_b32 m0, s60
	s_nop 0
	buffer_load_dwordx4 v64, s[8:11], s76 offen lds
	s_nop 0
	s_mov_b32 m0, s70
	s_nop 0
	buffer_load_dwordx4 v65, s[8:11], s76 offen lds
	s_barrier
	s_waitcnt lgkmcnt(0)
	s_barrier
	s_mov_b32 m0, s61
	s_nop 0
	buffer_load_dwordx4 v70, s[4:7], s77 offen lds
	s_nop 0
	s_mov_b32 m0, s71
	s_nop 0
	buffer_load_dwordx4 v70, s[4:7], s78 offen lds
	s_waitcnt vmcnt(10)
	s_barrier
	s_barrier
	s_mov_b32 s72, s74
	s_mov_b32 s75, s73
	s_cbranch_scc0 .LBB0_1510
	s_waitcnt vmcnt(0)
	s_cmpk_lt_u32 s15, 0x100
	s_cbranch_scc0 .LBB0_1513
	s_barrier

; #define G_WAIT_V(n) asm volatile("s_waitcnt vmcnt(" #n ")" ::: "memory")
; #define G_BAR() __builtin_amdgcn_s_barrier()
; #define G_SCHED() __builtin_amdgcn_sched_barrier(0)
; #define D_STAGE_A(slot, half, kt) D_STAGE(rsA, voffA, slot, half, kt)
; #define D_STAGE_B(slot, half, kt) D_STAGE(rsB, voffB, slot, half, kt)
; #define D_LDA(dst, slot) do { _Pragma("unroll") for (int m = 0; m < 4; ++m) _Pragma("unroll") for (int k = 0; k < 2; ++k) \
;     dst[m][k] = *(const LDS_AS bf16x8*)(lds + (slot) + aoff + m * 2048 + k * 1024); } while (0)
; #define D_LDB(dst, slot) do { _Pragma("unroll") for (int n = 0; n < 2; ++n) _Pragma("unroll") for (int k = 0; k < 2; ++k) \
;     dst[n][k] = *(const LDS_AS bf16x8*)(lds + (slot) + boff + n * 2048 + k * 1024); } while (0)
; #define D_MMA(ai, bj, At, Bf) do { __builtin_amdgcn_s_setprio(1); _Pragma("unroll") for (int m = 0; m < 4; ++m) _Pragma("unroll") for (int n = 0; n < 2; ++n) _Pragma("unroll") for (int k = 0; k < 2; ++k) \
;     acc[ai][bj][m][n] = __builtin_amdgcn_mfma_f32_16x16x32_bf16(Bf[n][k], At[m][k], acc[ai][bj][m][n], 0, 0, 0); __builtin_amdgcn_s_setprio(0); } while (0)
; #define D_WAIT_L(n) asm volatile("s_waitcnt lgkmcnt(" #n ")" ::: "memory")
; #define D_STAGE_A(slot, half, kt) D_STAGE(rsA, voffA, slot, half, kt)
; #define D_STAGE_B(slot, half, kt) do { _Pragma("unroll") for (int _i = 0; _i < 2; ++_i) { const unsigned _m0 = ldsw + (unsigned)((slot) + _i * 8192); const unsigned _so = (unsigned)(kt) * 128u + (half) * bt_half + _i * bt_piece; \
;     asm volatile("s_mov_b32 m0, %0\n\ts_nop 4\n\tbuffer_load_dwordx4 %1, %2, %3 offen lds" :: "s"(_m0), "v"(voffB0), "s"(rsB), "s"(_so) : "m0", "memory"); } } while (0)
;     ...
;     D_LDB(B0, G_SB(0, 0)); G_SCHED(); D_LDA(At, G_SA(0, 0)); D_STAGE_A(G_SA(1, 1), 1, t1);
;     D_WAIT_L(8); G_BAR(); D_WAIT_L(0); G_SCHED(); D_MMA(0, 0, At, B0); G_BAR(); G_SCHED();
;     D_LDB(B1, G_SB(0, 1)); D_STAGE_B(G_SB(0, 0), 0, t2);
;     G_BAR(); D_WAIT_L(0); G_SCHED(); D_MMA(0, 1, At, B1); G_BAR(); G_SCHED();
;     D_LDA(At, G_SA(0, 1)); D_STAGE_A(G_SA(0, 0), 0, t2);
;     G_BAR(); D_WAIT_L(0); G_SCHED(); D_MMA(1, 0, At, B0); G_BAR(); G_SCHED();
;     D_STAGE_B(G_SB(0, 1), 1, t2);
;     G_WAIT_V(6); G_BAR(); G_SCHED(); D_MMA(1, 1, At, B1); G_BAR(); G_SCHED();
;     D_LDB(B0, G_SB(1, 0)); G_SCHED(); D_LDA(At, G_SA(1, 0)); D_STAGE_A(G_SA(0, 1), 1, t2);
.LBB0_1701:
	s_add_i32 s68, 0, 0x10010
	s_nop 0
	v_add_u32_e32 v73, s68, v68
	s_nop 0
	v_add_u32_e32 v86, s68, v69
	ds_read_b128 v[74:77], v73
	ds_read_b128 v[82:85], v73 offset:2048
	ds_read_b128 v[78:81], v86
	s_nop 0
	ds_read_b128 v[86:89], v86 offset:2048
	s_add_i32 s38, s66, 1
	s_add_i32 s65, s66, 3
	s_add_i32 s64, s66, 2
	s_add_i32 s73, 0, 0x14010
	s_cmp_lt_u32 s66, 14
	s_cselect_b32 s67, s64, s66
	s_cselect_b32 s38, s65, s38
	s_lshl_b32 s72, s67, 7
	s_lshl_b32 s67, s38, 7
	s_add_i32 s74, s72, 0x20000
	s_add_i32 s75, s72, 0x40000
	s_add_i32 s76, s72, 0x60000
	s_add_i32 s77, 0, 0x18010
	s_add_i32 s71, 0, 0x1c010
	s_add_i32 s70, s67, 0x20000
	s_add_i32 s68, s67, 0x40000
	s_add_i32 s69, s67, 0x60000
	s_add_i32 s65, s63, 0x100
	s_cmp_gt_u32 s66, 13
	s_nop 0
	ds_read_b128 v[90:93], v71 offset:16
	s_nop 0
	ds_read_b128 v[98:101], v71 offset:2064
	ds_read_b128 v[94:97], v72 offset:16
	s_nop 0
	ds_read_b128 v[102:105], v72 offset:2064
	s_nop 0
	ds_read_b128 v[106:109], v71 offset:4112
	s_nop 0
	ds_read_b128 v[114:117], v71 offset:6160
	ds_read_b128 v[110:113], v72 offset:4112
	s_nop 0
	ds_read_b128 v[118:121], v72 offset:6160
	s_waitcnt lgkmcnt(12)
	s_mov_b32 m0, s24
	s_nop 0
	buffer_load_dwordx4 v66, s[8:11], s63 offen lds
	s_nop 0
	s_mov_b32 m0, s51
	s_nop 0
	buffer_load_dwordx4 v67, s[8:11], s63 offen lds
	s_waitcnt lgkmcnt(8)
	s_waitcnt vmcnt(10)
	s_barrier
	s_nop 0
	s_setprio 1
	s_waitcnt lgkmcnt(4)
	v_mfma_scale_f32_16x16x128_f8f6f4 v[40:43], v[74:81], v[98:105], v[40:43], v165, v164 op_sel_hi:[0,0,0]
	v_mfma_scale_f32_16x16x128_f8f6f4 v[32:35], v[82:89], v[98:105], v[32:35], v165, v164 op_sel_hi:[0,0,0]
	s_waitcnt lgkmcnt(1)
	v_mfma_scale_f32_16x16x128_f8f6f4 v[24:27], v[74:81], v[106:113], v[24:27], v165, v164 op_sel_hi:[0,0,0]
	v_mfma_scale_f32_16x16x128_f8f6f4 v[16:19], v[82:89], v[106:113], v[16:19], v165, v164 op_sel_hi:[0,0,0]
	s_waitcnt lgkmcnt(0)
	v_mfma_scale_f32_16x16x128_f8f6f4 v[8:11], v[74:81], v[114:121], v[8:11], v165, v164 op_sel_hi:[0,0,0]
	s_nop 0
	v_mfma_scale_f32_16x16x128_f8f6f4 v[122:125], v[74:81], v[90:97], v[48:51], v165, v164 op_sel_hi:[0,0,0]
	v_mfma_scale_f32_16x16x128_f8f6f4 v[126:129], v[82:89], v[90:97], v[52:55], v165, v164 op_sel_hi:[0,0,0]
	v_mfma_scale_f32_16x16x128_f8f6f4 v[130:133], v[82:89], v[114:121], v[0:3], v165, v164 op_sel_hi:[0,0,0]
	s_setprio 0
	s_barrier
	s_nop 4
	v_add_u32_e32 v0, s73, v68
	v_add_u32_e32 v1, s73, v69
	ds_read_b128 v[48:51], v0
	ds_read_b128 v[74:77], v0 offset:2048
	ds_read_b128 v[52:55], v1
	ds_read_b128 v[78:81], v1 offset:2048
	s_mov_b32 m0, s25
	s_nop 0
	buffer_load_dwordx4 v70, s[4:7], s72 offen lds
	s_nop 0
	s_mov_b32 m0, s54
	s_nop 0
	buffer_load_dwordx4 v70, s[4:7], s74 offen lds
	s_waitcnt vmcnt(10)
	s_barrier
	s_nop 0
	s_setprio 1
	s_waitcnt lgkmcnt(1)
	v_mfma_scale_f32_16x16x128_f8f6f4 v[44:47], v[48:55], v[98:105], v[44:47], v165, v164 op_sel_hi:[0,0,0]
	s_waitcnt lgkmcnt(0)
	v_mfma_scale_f32_16x16x128_f8f6f4 v[36:39], v[74:81], v[98:105], v[36:39], v165, v164 op_sel_hi:[0,0,0]
	v_mfma_scale_f32_16x16x128_f8f6f4 v[28:31], v[48:55], v[106:113], v[28:31], v165, v164 op_sel_hi:[0,0,0]
	v_mfma_scale_f32_16x16x128_f8f6f4 v[20:23], v[74:81], v[106:113], v[20:23], v165, v164 op_sel_hi:[0,0,0]
	v_mfma_scale_f32_16x16x128_f8f6f4 v[12:15], v[48:55], v[114:121], v[12:15], v165, v164 op_sel_hi:[0,0,0]
	v_mfma_scale_f32_16x16x128_f8f6f4 v[134:137], v[48:55], v[90:97], v[60:63], v165, v164 op_sel_hi:[0,0,0]
	v_mfma_scale_f32_16x16x128_f8f6f4 v[138:141], v[74:81], v[90:97], v[56:59], v165, v164 op_sel_hi:[0,0,0]
	v_mfma_scale_f32_16x16x128_f8f6f4 v[146:149], v[74:81], v[114:121], v[4:7], v165, v164 op_sel_hi:[0,0,0]
	s_setprio 0
	s_barrier
	s_mov_b32 m0, s15
	s_nop 0
	buffer_load_dwordx4 v64, s[8:11], s72 offen lds
	s_nop 0
	s_mov_b32 m0, s55
	s_nop 0
	buffer_load_dwordx4 v65, s[8:11], s72 offen lds
	s_barrier
; #define G_WAIT_V(n) asm volatile("s_waitcnt vmcnt(" #n ")" ::: "memory")
; #define G_BAR() __builtin_amdgcn_s_barrier()
; #define G_SCHED() __builtin_amdgcn_sched_barrier(0)
; #define D_STAGE_A(slot, half, kt) D_STAGE(rsA, voffA, slot, half, kt)
; #define D_STAGE_B(slot, half, kt) D_STAGE(rsB, voffB, slot, half, kt)
; #define D_LDA(dst, slot) do { _Pragma("unroll") for (int m = 0; m < 4; ++m) _Pragma("unroll") for (int k = 0; k < 2; ++k) \
;     dst[m][k] = *(const LDS_AS bf16x8*)(lds + (slot) + aoff + m * 2048 + k * 1024); } while (0)
; #define D_LDB(dst, slot) do { _Pragma("unroll") for (int n = 0; n < 2; ++n) _Pragma("unroll") for (int k = 0; k < 2; ++k) \
;     dst[n][k] = *(const LDS_AS bf16x8*)(lds + (slot) + boff + n * 2048 + k * 1024); } while (0)
; #define D_MMA(ai, bj, At, Bf) do { __builtin_amdgcn_s_setprio(1); _Pragma("unroll") for (int m = 0; m < 4; ++m) _Pragma("unroll") for (int n = 0; n < 2; ++n) _Pragma("unroll") for (int k = 0; k < 2; ++k) \
;     acc[ai][bj][m][n] = __builtin_amdgcn_mfma_f32_16x16x32_bf16(Bf[n][k], At[m][k], acc[ai][bj][m][n], 0, 0, 0); __builtin_amdgcn_s_setprio(0); } while (0)
; #define D_WAIT_L(n) asm volatile("s_waitcnt lgkmcnt(" #n ")" ::: "memory")
; #define D_STAGE_A(slot, half, kt) D_STAGE(rsA, voffA, slot, half, kt)
; #define D_STAGE_B(slot, half, kt) do { _Pragma("unroll") for (int _i = 0; _i < 2; ++_i) { const unsigned _m0 = ldsw + (unsigned)((slot) + _i * 8192); const unsigned _so = (unsigned)(kt) * 128u + (half) * bt_half + _i * bt_piece; \
;     asm volatile("s_mov_b32 m0, %0\n\ts_nop 4\n\tbuffer_load_dwordx4 %1, %2, %3 offen lds" :: "s"(_m0), "v"(voffB0), "s"(rsB), "s"(_so) : "m0", "memory"); } } while (0)
; #define D_WAIT_L(n) asm volatile("s_waitcnt lgkmcnt(" #n ")" ::: "memory")
;     ...
;     D_LDB(B0, G_SB(1, 0)); G_SCHED(); D_LDA(At, G_SA(1, 0)); D_STAGE_A(G_SA(0, 1), 1, t2);
;     D_WAIT_L(8); G_BAR(); D_WAIT_L(0); G_SCHED(); D_MMA(0, 0, At, B0); G_BAR(); G_SCHED();
;     D_LDB(B1, G_SB(1, 1)); D_STAGE_B(G_SB(1, 0), 0, t3);
;     G_BAR(); D_WAIT_L(0); G_SCHED(); D_MMA(0, 1, At, B1); G_BAR(); G_SCHED();
;     D_LDA(At, G_SA(1, 1)); D_STAGE_A(G_SA(1, 0), 0, t3);
;     G_BAR(); D_WAIT_L(0); G_SCHED(); D_MMA(1, 0, At, B0); G_BAR(); G_SCHED();
;     D_STAGE_B(G_SB(1, 1), 1, t3);
;     G_WAIT_V(6); G_BAR(); G_SCHED(); D_MMA(1, 1, At, B1); G_BAR(); G_SCHED();
;   }
	s_waitcnt lgkmcnt(0)
	s_barrier
	s_mov_b32 m0, s26
	s_nop 0
	buffer_load_dwordx4 v70, s[4:7], s75 offen lds
	s_nop 0
	s_mov_b32 m0, s58
	s_nop 0
	buffer_load_dwordx4 v70, s[4:7], s76 offen lds
	s_waitcnt vmcnt(10)
	s_barrier
	s_barrier
	v_add_u32_e32 v4, s77, v68
	v_add_u32_e32 v48, s77, v69
	ds_read_b128 v[0:3], v4
	ds_read_b128 v[56:59], v4 offset:2048
	ds_read_b128 v[4:7], v48
	ds_read_b128 v[60:63], v48 offset:2048
	ds_read_b128 v[74:77], v71 offset:32784
	ds_read_b128 v[82:85], v71 offset:34832
	ds_read_b128 v[78:81], v72 offset:32784
	ds_read_b128 v[86:89], v72 offset:34832
	ds_read_b128 v[90:93], v71 offset:36880
	ds_read_b128 v[98:101], v71 offset:38928
	ds_read_b128 v[94:97], v72 offset:36880
	ds_read_b128 v[102:105], v72 offset:38928
	s_mov_b32 m0, s27
	s_nop 0
	buffer_load_dwordx4 v66, s[8:11], s72 offen lds
	s_nop 0
	s_mov_b32 m0, s59
	s_nop 0
	buffer_load_dwordx4 v67, s[8:11], s72 offen lds
	s_waitcnt lgkmcnt(8)
	s_waitcnt vmcnt(10)
	s_barrier
	s_nop 0
	s_setprio 1
	s_waitcnt lgkmcnt(5)
	v_mfma_scale_f32_16x16x128_f8f6f4 v[48:51], v[0:7], v[74:81], v[122:125], v165, v164 op_sel_hi:[0,0,0]
	v_mfma_scale_f32_16x16x128_f8f6f4 v[52:55], v[56:63], v[74:81], v[126:129], v165, v164 op_sel_hi:[0,0,0]
	s_waitcnt lgkmcnt(4)
	v_mfma_scale_f32_16x16x128_f8f6f4 v[40:43], v[0:7], v[82:89], v[40:43], v165, v164 op_sel_hi:[0,0,0]
	v_mfma_scale_f32_16x16x128_f8f6f4 v[32:35], v[56:63], v[82:89], v[32:35], v165, v164 op_sel_hi:[0,0,0]
	s_waitcnt lgkmcnt(1)
	v_mfma_scale_f32_16x16x128_f8f6f4 v[24:27], v[0:7], v[90:97], v[24:27], v165, v164 op_sel_hi:[0,0,0]
	v_mfma_scale_f32_16x16x128_f8f6f4 v[16:19], v[56:63], v[90:97], v[16:19], v165, v164 op_sel_hi:[0,0,0]
	s_waitcnt lgkmcnt(0)
	v_mfma_scale_f32_16x16x128_f8f6f4 v[8:11], v[0:7], v[98:105], v[8:11], v165, v164 op_sel_hi:[0,0,0]
	v_mfma_scale_f32_16x16x128_f8f6f4 v[0:3], v[56:63], v[98:105], v[130:133], v165, v164 op_sel_hi:[0,0,0]
	s_setprio 0
	s_barrier
	v_add_u32_e32 v4, s71, v68
	v_add_u32_e32 v5, s71, v69
	ds_read_b128 v[106:109], v4
	ds_read_b128 v[114:117], v4 offset:2048
	ds_read_b128 v[110:113], v5
	ds_read_b128 v[118:121], v5 offset:2048
	s_mov_b32 m0, s39
	s_nop 0
	buffer_load_dwordx4 v70, s[4:7], s67 offen lds
	s_nop 0
	s_mov_b32 m0, s60
	s_nop 0
	buffer_load_dwordx4 v70, s[4:7], s70 offen lds
	s_waitcnt vmcnt(10)
	s_barrier
	s_nop 0
	s_setprio 1
	s_waitcnt lgkmcnt(1)
	v_mfma_scale_f32_16x16x128_f8f6f4 v[60:63], v[106:113], v[74:81], v[134:137], v165, v164 op_sel_hi:[0,0,0]
	s_waitcnt lgkmcnt(0)
	v_mfma_scale_f32_16x16x128_f8f6f4 v[56:59], v[114:121], v[74:81], v[138:141], v165, v164 op_sel_hi:[0,0,0]
	v_mfma_scale_f32_16x16x128_f8f6f4 v[44:47], v[106:113], v[82:89], v[44:47], v165, v164 op_sel_hi:[0,0,0]
	v_mfma_scale_f32_16x16x128_f8f6f4 v[36:39], v[114:121], v[82:89], v[36:39], v165, v164 op_sel_hi:[0,0,0]
	v_mfma_scale_f32_16x16x128_f8f6f4 v[28:31], v[106:113], v[90:97], v[28:31], v165, v164 op_sel_hi:[0,0,0]
	v_mfma_scale_f32_16x16x128_f8f6f4 v[20:23], v[114:121], v[90:97], v[20:23], v165, v164 op_sel_hi:[0,0,0]
	v_mfma_scale_f32_16x16x128_f8f6f4 v[12:15], v[106:113], v[98:105], v[12:15], v165, v164 op_sel_hi:[0,0,0]
	v_mfma_scale_f32_16x16x128_f8f6f4 v[4:7], v[114:121], v[98:105], v[146:149], v165, v164 op_sel_hi:[0,0,0]
	s_setprio 0
	s_barrier
	s_mov_b32 m0, s49
	s_nop 0
	buffer_load_dwordx4 v64, s[8:11], s67 offen lds
	s_nop 0
	s_mov_b32 m0, s61
	s_nop 0
	buffer_load_dwordx4 v65, s[8:11], s67 offen lds
	s_barrier
	s_waitcnt lgkmcnt(0)
	s_barrier
	s_mov_b32 m0, s50
	s_nop 0
	buffer_load_dwordx4 v70, s[4:7], s68 offen lds
	s_nop 0
	s_mov_b32 m0, s62
	s_nop 0
	buffer_load_dwordx4 v70, s[4:7], s69 offen lds
	s_waitcnt vmcnt(10)
	s_barrier
	s_barrier
	s_mov_b32 s63, s65
	s_mov_b32 s66, s64
	s_cbranch_scc0 .LBB0_1701
	s_waitcnt vmcnt(0)
	s_cmpk_lt_u32 s13, 0x100
	s_cbranch_scc0 .LBB0_1704
	s_barrier
